# attention round prologue (masked and dilated): full vmcnt(0) drain before the tile loop replaced by vmcnt(8) (only the Q fragment loads are needed; the staged K/V tiles are covered by the loop's count
# speedup vs baseline: 1.0076x; 1.0076x over previous
.LBB0_1633:
	s_or_b64 exec, exec, s[4:5]
	v_mov_b32_e32 v16, v3
	v_mov_b32_e32 v17, v3
	v_mov_b32_e32 v2, v3
	v_mov_b32_e32 v4, v3
	v_mov_b32_e32 v5, v3
	v_mov_b32_e32 v6, v3
	v_mov_b32_e32 v7, v3
	v_mov_b32_e32 v8, v3
	v_mov_b32_e32 v9, v3
	v_mov_b32_e32 v10, v3
	v_mov_b32_e32 v11, v3
	v_mov_b32_e32 v12, v3
	v_mov_b32_e32 v13, v3
	v_mov_b32_e32 v14, v3
	v_mov_b32_e32 v15, v3
	v_mov_b64_e32 v[34:35], v[16:17]
	v_mov_b64_e32 v[32:33], v[14:15]
	v_mov_b64_e32 v[30:31], v[12:13]
	v_mov_b64_e32 v[28:29], v[10:11]
	v_mov_b64_e32 v[26:27], v[8:9]
	v_mov_b64_e32 v[24:25], v[6:7]
	v_mov_b64_e32 v[22:23], v[4:5]
	v_mov_b64_e32 v[20:21], v[2:3]
	v_mov_b64_e32 v[18:19], v[16:17]
	s_mov_b32 s16, 0
	v_mov_b32_e32 v90, 0xf149f2ca
	v_mov_b32_e32 v110, 0
	s_movk_i32 s50, 0xa0
	s_mov_b64 s[4:5], 0
	v_mov_b64_e32 v[88:89], v[82:83]
	v_mov_b32_e32 v111, v109
	v_mov_b32_e32 v112, v101
	v_mov_b32_e32 v113, v69
	v_mov_b64_e32 v[16:17], v[14:15]
	v_mov_b64_e32 v[14:15], v[12:13]
	v_mov_b64_e32 v[12:13], v[10:11]
	v_mov_b64_e32 v[10:11], v[8:9]
	v_mov_b64_e32 v[8:9], v[6:7]
	v_mov_b64_e32 v[6:7], v[4:5]
	v_mov_b64_e32 v[4:5], v[2:3]
	s_mov_b32 s17, 0
	v_and_b32_e32 v195, 64, v214
	v_xor_b32_e32 v194, 32, v214
	v_add_u32_e32 v195, 64, v195
	v_cmp_lt_i32_e32 vcc, v194, v195
	s_nop 1
	v_cndmask_b32_e32 v194, v214, v194, vcc
	v_lshlrev_b32_e32 v194, 2, v194
	s_waitcnt vmcnt(8) lgkmcnt(0)
	s_barrier
	s_branch .LBB0_1636

.LBB0_1687:
	s_or_b64 exec, exec, s[22:23]
	v_mov_b32_e32 v16, v3
	v_mov_b32_e32 v17, v3
	v_mov_b32_e32 v2, v3
	v_mov_b32_e32 v4, v3
	v_mov_b32_e32 v5, v3
	v_mov_b32_e32 v6, v3
	v_mov_b32_e32 v7, v3
	v_mov_b32_e32 v8, v3
	v_mov_b32_e32 v9, v3
	v_mov_b32_e32 v10, v3
	v_mov_b32_e32 v11, v3
	v_mov_b32_e32 v12, v3
	v_mov_b32_e32 v13, v3
	v_mov_b32_e32 v14, v3
	v_mov_b32_e32 v15, v3
	v_mov_b64_e32 v[34:35], v[16:17]
	v_mov_b64_e32 v[32:33], v[14:15]
	v_mov_b64_e32 v[30:31], v[12:13]
	v_mov_b64_e32 v[28:29], v[10:11]
	v_mov_b64_e32 v[26:27], v[8:9]
	v_mov_b64_e32 v[24:25], v[6:7]
	v_mov_b64_e32 v[22:23], v[4:5]
	v_mov_b64_e32 v[20:21], v[2:3]
	v_mov_b64_e32 v[18:19], v[16:17]
	s_mov_b32 s46, 0
	v_mov_b32_e32 v158, 0xf149f2ca
	v_mov_b32_e32 v157, 0
	s_movk_i32 s47, 0x21f
	s_mov_b32 s48, 63
	s_mov_b64 s[22:23], 0
	v_mov_b64_e32 v[128:129], v[122:123]
	v_mov_b32_e32 v156, v153
	v_mov_b64_e32 v[16:17], v[14:15]
	v_mov_b64_e32 v[14:15], v[12:13]
	v_mov_b64_e32 v[12:13], v[10:11]
	v_mov_b64_e32 v[10:11], v[8:9]
	v_mov_b64_e32 v[8:9], v[6:7]
	v_mov_b64_e32 v[6:7], v[4:5]
	v_mov_b64_e32 v[4:5], v[2:3]
	s_mov_b32 s49, 0
	s_waitcnt vmcnt(8) lgkmcnt(0)
	s_barrier
	s_branch .LBB0_1691
